# scan helper waves run at s_setprio 2 during their chunk loop (they bound the chunk time; the scan waves have slack)
# speedup vs baseline: 1.0053x; 1.0053x over previous
; __device__ __forceinline__ void scan_unit(Frame& F, const Args& a, int layer, int unit) {
;     ...
;         const int ht = tid - 256, tl = ht >> 3, c8 = ht & 7, ch = hh * 64 + c8 * 8;
;         const int pr = ht >> 4, c4 = ht & 15, chp = hh * 64 + c4 * 4;
;         const size_t po = (size_t)layer * 1024 + ch, pop = (size_t)layer * 1024 + chp;
;         struct HelpIn { v2u r0, k0, v0, e0, a0, r1, k1, v1, e1, a1, k2, v2, e2, a2, k3; v4u gt; };
;         HelpIn cur, nxt;
;     ...
;         unsigned long long ph_act = 0ull;
;     ...
;         HELP_LOAD(cur, 0, -2);
;         for (int it = 0; it < NCH + 2; ++it) {
;     ...
;             const unsigned long long ph0 = __builtin_amdgcn_s_memtime();
;     ...
;             HELP_LOAD(nxt, it + 1, it - 1);
.LBB0_1318:
	v_readlane_b32 s2, v253, 41
	v_readlane_b32 s3, v253, 42
	v_mbcnt_lo_u32_b32 v1, -1, 0
	v_mbcnt_hi_u32_b32 v1, -1, v1
	s_mov_b64 s[0:1], -1
	v_add_u32_e32 v125, s27, v1
	s_and_b64 vcc, exec, s[2:3]
	v_and_b32_e32 v124, 15, v1
	s_cbranch_vccz .LBB0_1336
	s_add_u32 s36, s18, 0x1a400000
	s_addc_u32 s37, s19, 0
	s_add_u32 s6, s18, 0x3c400000
	s_addc_u32 s7, s19, 0
	s_add_u32 s20, s18, 0x38400000
	s_addc_u32 s21, s19, 0
	v_add_u32_e32 v20, 0xffffff00, v125
	v_and_b32_e32 v126, 7, v1
	s_lshl_b32 s1, s22, 6
	s_ashr_i32 s0, s22, 4
	s_and_b32 s1, s1, 0x3c0
	v_lshlrev_b32_e32 v21, 3, v126
	v_ashrrev_i32_e32 v22, 4, v20
	v_lshlrev_b32_e32 v127, 2, v124
	v_or_b32_e32 v7, s1, v21
	v_or_b32_e32 v16, s1, v127
	v_lshlrev_b32_e32 v2, 1, v22
	s_ashr_i32 s1, s0, 31
	s_lshl_b64 s[2:3], s[0:1], 12
	v_ashrrev_i32_e32 v3, 31, v2
	v_lshl_add_u64 v[10:11], s[2:3], 0, v[2:3]
	v_mov_b64_e32 v[12:13], s[36:37]
	s_movk_i32 s23, 0x1800
	v_mad_u64_u32 v[14:15], s[36:37], v10, s23, v[12:13]
	v_or_b32_e32 v4, s60, v16
	v_mad_i32_i24 v15, v11, s23, v15
	v_lshlrev_b32_e32 v16, 1, v16
	v_mov_b32_e32 v17, v0
	v_lshl_add_u64 v[14:15], v[14:15], 0, v[16:17]
	global_load_dwordx2 v[82:83], v[14:15], off
	global_load_dwordx2 v[100:101], v[14:15], off offset:2048
	v_add_co_u32_e32 v14, vcc, s9, v14
	v_lshlrev_b64 v[10:11], 11, v[10:11]
	s_nop 0
	v_addc_co_u32_e32 v15, vcc, 0, v15, vcc
	global_load_dwordx2 v[80:81], v[14:15], off
	v_lshl_add_u64 v[14:15], s[20:21], 0, v[10:11]
	v_lshl_add_u64 v[10:11], s[6:7], 0, v[10:11]
	v_lshl_add_u64 v[14:15], v[14:15], 0, v[16:17]
	v_lshl_add_u64 v[10:11], v[10:11], 0, v[16:17]
	global_load_dwordx2 v[78:79], v[14:15], off
	global_load_dwordx2 v[84:85], v[10:11], off
	v_or_b32_e32 v10, 1, v2
	v_ashrrev_i32_e32 v11, 31, v10
	v_lshl_add_u64 v[14:15], s[2:3], 0, v[10:11]
	v_mad_u64_u32 v[18:19], s[36:37], v14, s23, v[12:13]
	v_mad_i32_i24 v19, v15, s23, v19
	v_lshl_add_u64 v[18:19], v[18:19], 0, v[16:17]
	global_load_dwordx2 v[88:89], v[18:19], off
	global_load_dwordx2 v[102:103], v[18:19], off offset:2048
	v_add_co_u32_e32 v18, vcc, s9, v18
	v_lshlrev_b64 v[14:15], 11, v[14:15]
	s_nop 0
	v_addc_co_u32_e32 v19, vcc, 0, v19, vcc
	global_load_dwordx2 v[92:93], v[18:19], off
	v_lshl_add_u64 v[18:19], s[20:21], 0, v[14:15]
	v_lshl_add_u64 v[14:15], s[6:7], 0, v[14:15]
	v_lshl_add_u64 v[18:19], v[18:19], 0, v[16:17]
	v_lshl_add_u64 v[14:15], v[14:15], 0, v[16:17]
	global_load_dwordx2 v[86:87], v[18:19], off
	global_load_dwordx2 v[90:91], v[14:15], off
	v_add_u32_e32 v14, 2, v2
	v_ashrrev_i32_e32 v15, 31, v14
	v_lshl_add_u64 v[14:15], s[2:3], 0, v[14:15]
	v_mad_u64_u32 v[18:19], s[36:37], v14, s23, v[12:13]
	v_mad_i32_i24 v19, v15, s23, v19
	v_lshl_add_u64 v[18:19], v[18:19], 0, v[16:17]
	global_load_dwordx2 v[104:105], v[18:19], off offset:2048
	v_add_co_u32_e32 v18, vcc, s9, v18
	v_lshlrev_b64 v[14:15], 11, v[14:15]
	s_nop 0
	v_addc_co_u32_e32 v19, vcc, 0, v19, vcc
	global_load_dwordx2 v[98:99], v[18:19], off
	v_lshl_add_u64 v[18:19], s[20:21], 0, v[14:15]
	v_lshl_add_u64 v[14:15], s[6:7], 0, v[14:15]
	v_lshl_add_u64 v[14:15], v[14:15], 0, v[16:17]
	global_load_dwordx2 v[96:97], v[14:15], off
	v_add_u32_e32 v14, 3, v2
	v_ashrrev_i32_e32 v15, 31, v14
	v_lshl_add_u64 v[14:15], s[2:3], 0, v[14:15]
	v_mad_u64_u32 v[12:13], s[6:7], v14, s23, v[12:13]
	v_mad_i32_i24 v13, v15, s23, v13
	v_lshl_add_u64 v[18:19], v[18:19], 0, v[16:17]
	v_lshl_add_u64 v[12:13], v[12:13], 0, v[16:17]
	global_load_dwordx2 v[94:95], v[18:19], off
	global_load_dwordx2 v[106:107], v[12:13], off offset:2048
	v_ashrrev_i32_e32 v6, 3, v20
	v_or_b32_e32 v8, s60, v7
	v_lshlrev_b32_e32 v12, 1, v7
	v_ashrrev_i32_e32 v7, 31, v6
	v_lshl_add_u64 v[14:15], s[2:3], 0, v[6:7]
	v_lshl_or_b32 v128, v6, 6, v21
	v_and_b32_e32 v6, 3, v1
	v_mov_b32_e32 v13, v0
	s_add_i32 s2, 0, 0x17200
	v_lshlrev_b32_e32 v135, 7, v6
	v_lshlrev_b32_e32 v137, 4, v6
	v_lshlrev_b32_e32 v6, 1, v1
	v_lshl_add_u64 v[12:13], s[18:19], 0, v[12:13]
	v_lshl_add_u32 v129, v128, 2, s2
	v_and_b32_e32 v138, 8, v6
	s_movk_i32 s2, 0x50
	v_lshlrev_b64 v[6:7], 11, v[14:15]
	v_mul_lo_u32 v139, v22, s2
	v_lshl_add_u64 v[6:7], v[12:13], 0, v[6:7]
	s_mov_b64 s[2:3], 0x40400000
	v_lshl_add_u64 v[30:31], v[6:7], 0, s[2:3]
	s_lshl_b32 s2, s5, 1
	v_lshlrev_b32_e32 v17, 3, v124
	s_and_b32 s2, s2, 0x780
	v_or_b32_e32 v42, s2, v17
	s_mul_i32 s2, s0, 0x1800000
	v_mov_b32_e32 v5, v0
	v_readlane_b32 s44, v251, 18
	s_mul_hi_i32 s3, s0, 0x1800000
	s_add_u32 s2, s18, s2
	v_readlane_b32 s50, v251, 24
	v_readlane_b32 s51, v251, 25
	v_readlane_b32 s52, v251, 26
	v_readlane_b32 s53, v251, 27
	v_readlane_b32 s54, v251, 28
	v_readlane_b32 s55, v251, 29
	v_lshlrev_b64 v[4:5], 2, v[4:5]
	s_addc_u32 s3, s19, s3
	s_lshl_b64 s[0:1], s[0:1], 23
	v_mov_b32_e32 v9, v0
	v_lshl_add_u64 v[36:37], s[50:51], 0, v[4:5]
	v_lshl_add_u64 v[38:39], s[52:53], 0, v[4:5]
	v_lshl_add_u64 v[40:41], s[54:55], 0, v[4:5]
	v_mov_b64_e32 v[4:5], s[2:3]
	s_add_u32 s0, s18, s0
	v_and_b32_e32 v11, -8, v20
	v_bfe_u32 v16, v1, 2, 2
	v_and_b32_e32 v18, -16, v20
	v_bfe_u32 v19, v1, 1, 3
	v_lshlrev_b64 v[6:7], 2, v[8:9]
	v_readlane_b32 s56, v251, 30
	v_readlane_b32 s57, v251, 31
	v_readlane_b32 s58, v251, 32
	v_readlane_b32 s59, v251, 33
	v_mad_i64_i32 v[44:45], s[2:3], v2, s23, v[4:5]
	v_lshlrev_b64 v[2:3], 11, v[2:3]
	s_addc_u32 s1, s19, s1
	v_lshlrev_b32_e32 v130, 8, v22
	v_lshlrev_b32_e32 v131, 9, v22
	v_lshlrev_b32_e32 v132, 8, v10
	v_lshlrev_b32_e32 v133, 10, v22
	v_lshlrev_b32_e32 v134, 6, v124
	v_and_b32_e32 v136, 64, v17
	v_cmp_eq_u32_e64 s[40:41], 0, v124
	v_lshlrev_b32_e32 v140, 5, v10
	v_lshl_add_u64 v[32:33], s[56:57], 0, v[6:7]
	v_lshl_add_u64 v[34:35], s[58:59], 0, v[6:7]
	v_mov_b32_e32 v43, v0
	v_lshl_add_u64 v[46:47], s[0:1], 0, v[2:3]
	s_mov_b32 s0, -2
	v_lshlrev_b32_e32 v141, 2, v11
	v_lshlrev_b32_e32 v142, 3, v16
	v_lshlrev_b32_e32 v143, 2, v18
	v_lshlrev_b32_e32 v144, 2, v19
	v_readlane_b32 s45, v251, 19
	v_readlane_b32 s46, v251, 20
	v_readlane_b32 s47, v251, 21
	v_readlane_b32 s48, v251, 22
	v_readlane_b32 s49, v251, 23
	global_load_dwordx4 v[176:179], v[32:33], off
	global_load_dwordx4 v[180:183], v[32:33], off offset:16
	global_load_dwordx4 v[184:187], v[34:35], off
	global_load_dwordx4 v[188:191], v[34:35], off offset:16
	global_load_dwordx4 v[192:195], v[36:37], off
	global_load_dwordx4 v[196:199], v[38:39], off
	global_load_dwordx4 v[200:203], v[40:41], off
	s_waitcnt vmcnt(0)
	s_setprio 2
	s_branch .LBB0_1322

; __device__ __forceinline__ void scan_unit(Frame& F, const Args& a, int layer, int unit) {
;     ...
;             cur = nxt;
;     ...
;             asm volatile("s_waitcnt vmcnt(0) lgkmcnt(0)" ::: "memory"); ph_act += __builtin_amdgcn_s_memtime() - ph0;
;     ...
;             __syncthreads();
;         }
.LBB0_1335:
	s_setprio 0
	s_mov_b64 s[0:1], 0
